# v55 with the ten hot loop heads (GEMM K loops, attention tile loops) aligned to 64 bytes
# baseline (speedup 1.0000x reference)
.LBB0_1579:
	v_lshlrev_b32_e32 v36, 5, v179
	v_and_b32_e32 v36, 0x180, v36
	v_lshlrev_b32_e32 v38, 3, v179
	v_lshl_or_b32 v36, v98, 9, v36
	v_lshlrev_b32_e32 v37, 5, v187
	v_and_b32_e32 v38, 24, v38
	v_or3_b32 v36, v36, v37, v38
	v_lshlrev_b32_e32 v37, 6, v186
	v_and_or_b32 v209, v37, 64, v36
	v_bitop3_b32 v210, v36, 64, v37 bitop3:0x34
	v_and_b32_e32 v37, 7, v179
	v_and_b32_e32 v36, 30, v188
	v_lshlrev_b32_e32 v229, 10, v37
	v_lshlrev_b32_e32 v37, 4, v37
	v_lshl_or_b32 v200, v36, 11, v37
	v_lshrrev_b32_e32 v36, 1, v179
	v_and_b32_e32 v228, 28, v36
	v_lshlrev_b32_e32 v36, 3, v185
	v_and_b32_e32 v37, 4, v179
	v_and_or_b32 v36, v36, 24, v37
	v_lshlrev_b32_e32 v198, 2, v36
	v_bitop3_b32 v36, v179, 5, 7 bitop3:0x6c
	v_bfe_u32 v39, v188, 2, 3
	v_lshlrev_b32_e32 v37, 3, v36
	v_bitop3_b32 v39, v39, v179, 7 bitop3:0x78
	v_bitop3_b32 v36, v37, 28, v36 bitop3:0xc8
	v_lshlrev_b32_e32 v230, 4, v39
	v_lshlrev_b32_e32 v39, 2, v188
	v_lshlrev_b32_e32 v188, 2, v36
	v_bitop3_b32 v36, v179, 6, 7 bitop3:0x6c
	v_lshlrev_b32_e32 v37, 3, v36
	v_bitop3_b32 v36, v37, 28, v36 bitop3:0xc8
	s_lshl_b32 s4, s76, 10
	v_lshlrev_b32_e32 v186, 2, v36
	v_bitop3_b32 v36, v179, 7, v179 bitop3:0xc
	s_waitcnt lgkmcnt(0)
	s_barrier
	s_sub_i32 s17, 0, s4
	v_lshlrev_b32_e32 v37, 3, v36
	s_add_i32 s4, 0, 0x8000
	s_lshl_b32 s15, s76, 4
	v_mov_b32_e32 v177, v99
	v_add_u32_e32 v38, 0, v229
	v_and_b32_e32 v231, 8, v39
	v_bitop3_b32 v36, v37, 28, v36 bitop3:0xc8
	v_add_u32_e32 v205, s4, v209
	v_add_u32_e32 v67, s4, v210
	s_add_i32 s4, 0, 0x6000
	v_lshlrev_b32_e32 v35, 3, v175
	s_lshl_b32 s12, s40, 6
	s_mov_b32 s14, 3
	s_add_i32 s16, s41, 0
	v_lshl_add_u64 v[202:203], s[56:57], 0, v[176:177]
	v_and_b32_e32 v232, -2, v189
	v_add3_u32 v233, v38, v230, v231
	v_mov_b32_e32 v201, v99
	s_lshl_b32 s13, s78, 1
	v_mov_b32_e32 v199, v99
	v_xor_b32_e32 v196, 32, v198
	v_mov_b32_e32 v197, v99
	v_xor_b32_e32 v194, 64, v198
	v_mov_b32_e32 v195, v99
	v_xor_b32_e32 v192, 0x60, v198
	v_mov_b32_e32 v193, v99
	v_xor_b32_e32 v190, 16, v198
	v_mov_b32_e32 v191, v99
	v_mov_b32_e32 v189, v99
	v_mov_b32_e32 v187, v99
	v_lshlrev_b32_e32 v64, 2, v36
	v_mov_b32_e32 v65, v99
	v_cmp_eq_u32_e64 s[34:35], 0, v185
	v_mov_b32_e32 v175, v99
	v_mov_b32_e32 v179, v99
	v_mov_b32_e32 v185, v99
	v_add_u32_e32 v234, s4, v209
	v_add_u32_e32 v235, s4, v210
	s_add_i32 s18, s15, 0x80
	v_mov_b64_e32 v[240:241], s[92:93]
	v_mov_b64_e32 v[242:243], s[94:95]
	.p2alignl 6, 3212836864

.LBB0_1983:
	v_and_or_b32 v89, v189, 3, v187
	v_lshlrev_b32_e32 v89, 7, v89
	v_lshlrev_b32_e32 v87, 5, v87
	v_and_b32_e32 v88, 24, v88
	s_waitcnt lgkmcnt(0)
	s_barrier
	v_or3_b32 v87, v89, v87, v88
	v_lshlrev_b32_e32 v86, 6, v86
	v_and_or_b32 v177, v86, 64, v87
	v_bitop3_b32 v178, v87, 64, v86 bitop3:0x34
	s_cmp_lt_i32 s85, 3
	s_cbranch_scc1 .LBB0_2059
	v_mov_b32_e32 v149, v99
	v_ashrrev_i32_e32 v86, 6, v185
	v_and_b32_e32 v87, 7, v185
	v_lshl_add_u64 v[154:155], s[18:19], 0, v[148:149]
	v_and_b32_e32 v149, -2, v86
	v_and_b32_e32 v86, 30, v189
	v_lshl_add_u32 v88, v87, 10, 0
	v_lshlrev_b32_e32 v87, 4, v87
	v_lshl_or_b32 v156, v86, 11, v87
	v_lshlrev_b32_e32 v86, 3, v179
	v_and_b32_e32 v87, 4, v185
	v_and_or_b32 v86, v86, 24, v87
	v_lshlrev_b32_e32 v158, 2, v86
	v_bitop3_b32 v86, v185, 5, 7 bitop3:0x6c
	v_lshlrev_b32_e32 v87, 3, v86
	v_bitop3_b32 v86, v87, 28, v86 bitop3:0xc8
	v_lshlrev_b32_e32 v168, 2, v86
	v_bitop3_b32 v86, v185, 6, 7 bitop3:0x6c
	v_lshlrev_b32_e32 v87, 3, v86
	v_bitop3_b32 v86, v87, 28, v86 bitop3:0xc8
	v_lshlrev_b32_e32 v170, 2, v86
	v_bitop3_b32 v86, v185, 7, v185 bitop3:0xc
	v_bfe_u32 v89, v189, 2, 3
	v_lshlrev_b32_e32 v87, 3, v86
	s_add_i32 s4, 0, 0x4000
	v_bitop3_b32 v89, v89, v185, 7 bitop3:0x78
	v_lshlrev_b32_e32 v90, 2, v189
	v_bitop3_b32 v86, v87, 28, v86 bitop3:0xc8
	v_add_u32_e32 v200, s4, v177
	v_add_u32_e32 v201, s4, v178
	s_add_i32 s4, 0, 0x6000
	v_lshlrev_b32_e32 v89, 4, v89
	v_and_b32_e32 v90, 8, v90
	v_lshlrev_b32_e32 v172, 2, v86
	v_add_u32_e32 v202, s4, v177
	v_add_u32_e32 v203, s4, v178
	v_add_u32_e32 v86, s86, v187
	s_sub_i32 s4, s89, s86
	s_lshl_b32 s97, s90, 4
	s_lshl_b32 s2, s90, 11
	v_add3_u32 v198, v88, v89, v90
	v_mov_b32_e32 v157, v99
	s_lshl_b32 s3, s91, 1
	v_and_b32_e32 v199, 28, v186
	s_mov_b32 s76, 3
	v_mov_b32_e32 v159, v99
	v_xor_b32_e32 v160, 32, v158
	v_mov_b32_e32 v161, v99
	v_xor_b32_e32 v162, 64, v158
	v_mov_b32_e32 v163, v99
	v_xor_b32_e32 v164, 0x60, v158
	v_mov_b32_e32 v165, v99
	v_xor_b32_e32 v166, 16, v158
	v_mov_b32_e32 v167, v99
	v_mov_b32_e32 v169, v99
	v_mov_b32_e32 v171, v99
	v_mov_b32_e32 v173, v99
	s_mov_b32 s14, 0
	v_cmp_eq_u32_e64 s[36:37], 0, v179
	v_mov_b32_e32 v151, v99
	v_mov_b32_e32 v153, v99
	s_sub_i32 s56, s86, s89
	v_sub_u32_e32 v204, v86, v176
	s_add_i32 s6, s4, 0xffffff9f
	v_mov_b64_e32 v[240:241], s[92:93]
	v_mov_b64_e32 v[242:243], s[94:95]
	.p2alignl 6, 3212836864

.LBB0_2957:
	s_ashr_i32 s35, s16, 31
	s_mov_b32 s34, s16
	s_lshl_b64 s[34:35], s[34:35], 19
	s_add_u32 s34, s27, s34
	s_addc_u32 s35, s49, s35
	s_ashr_i32 s37, s17, 31
	s_mov_b32 s36, s17
	s_lshl_b64 s[36:37], s[36:37], 19
	s_add_u32 s36, s25, s36
	s_addc_u32 s37, s26, s37
	s_and_b64 s[42:43], s[18:19], exec
	s_cselect_b32 s57, s37, s41
	s_cselect_b32 s64, s36, s40
	s_add_u32 s65, s40, 0x100
	s_addc_u32 s76, s41, 0
	s_add_u32 s40, s38, 0x40080
	s_addc_u32 s41, s39, 0
	v_mov_b32_e32 v6, 0
	v_lshl_add_u64 v[2:3], s[40:41], 0, v[158:159]
	v_lshl_add_u64 v[140:141], s[40:41], 0, v[160:161]
	s_mov_b32 s78, -2
	s_mov_b64 s[40:41], 0
	v_mov_b32_e32 v7, v6
	v_mov_b32_e32 v8, v6
	v_mov_b32_e32 v9, v6
	v_mov_b32_e32 v10, v6
	v_mov_b32_e32 v11, v6
	v_mov_b32_e32 v12, v6
	v_mov_b32_e32 v13, v6
	v_mov_b32_e32 v24, v6
	v_mov_b32_e32 v25, v6
	v_mov_b32_e32 v26, v6
	v_mov_b32_e32 v27, v6
	v_mov_b32_e32 v28, v6
	v_mov_b32_e32 v29, v6
	v_mov_b32_e32 v30, v6
	v_mov_b32_e32 v31, v6
	v_mov_b32_e32 v40, v6
	v_mov_b32_e32 v41, v6
	v_mov_b32_e32 v42, v6
	v_mov_b32_e32 v43, v6
	v_mov_b32_e32 v44, v6
	v_mov_b32_e32 v45, v6
	v_mov_b32_e32 v46, v6
	v_mov_b32_e32 v47, v6
	v_mov_b32_e32 v56, v6
	v_mov_b32_e32 v57, v6
	v_mov_b32_e32 v58, v6
	v_mov_b32_e32 v59, v6
	v_mov_b32_e32 v60, v6
	v_mov_b32_e32 v61, v6
	v_mov_b32_e32 v62, v6
	v_mov_b32_e32 v63, v6
	v_mov_b32_e32 v14, v6
	v_mov_b32_e32 v15, v6
	v_mov_b32_e32 v16, v6
	v_mov_b32_e32 v17, v6
	v_mov_b32_e32 v18, v6
	v_mov_b32_e32 v19, v6
	v_mov_b32_e32 v20, v6
	v_mov_b32_e32 v21, v6
	v_mov_b32_e32 v32, v6
	v_mov_b32_e32 v33, v6
	v_mov_b32_e32 v34, v6
	v_mov_b32_e32 v35, v6
	v_mov_b32_e32 v36, v6
	v_mov_b32_e32 v37, v6
	v_mov_b32_e32 v38, v6
	v_mov_b32_e32 v39, v6
	v_mov_b32_e32 v48, v6
	v_mov_b32_e32 v49, v6
	v_mov_b32_e32 v50, v6
	v_mov_b32_e32 v51, v6
	v_mov_b32_e32 v52, v6
	v_mov_b32_e32 v53, v6
	v_mov_b32_e32 v54, v6
	v_mov_b32_e32 v55, v6
	v_mov_b32_e32 v64, v6
	v_mov_b32_e32 v65, v6
	v_mov_b32_e32 v66, v6
	v_mov_b32_e32 v67, v6
	v_mov_b32_e32 v68, v6
	v_mov_b32_e32 v69, v6
	v_mov_b32_e32 v70, v6
	v_mov_b32_e32 v71, v6
	v_mov_b32_e32 v72, v6
	v_mov_b32_e32 v73, v6
	v_mov_b32_e32 v74, v6
	v_mov_b32_e32 v75, v6
	v_mov_b32_e32 v76, v6
	v_mov_b32_e32 v77, v6
	v_mov_b32_e32 v78, v6
	v_mov_b32_e32 v79, v6
	v_mov_b32_e32 v88, v6
	v_mov_b32_e32 v89, v6
	v_mov_b32_e32 v90, v6
	v_mov_b32_e32 v91, v6
	v_mov_b32_e32 v92, v6
	v_mov_b32_e32 v93, v6
	v_mov_b32_e32 v94, v6
	v_mov_b32_e32 v95, v6
	v_mov_b32_e32 v108, v6
	v_mov_b32_e32 v109, v6
	v_mov_b32_e32 v110, v6
	v_mov_b32_e32 v111, v6
	v_mov_b32_e32 v112, v6
	v_mov_b32_e32 v113, v6
	v_mov_b32_e32 v114, v6
	v_mov_b32_e32 v115, v6
	v_mov_b32_e32 v124, v6
	v_mov_b32_e32 v125, v6
	v_mov_b32_e32 v126, v6
	v_mov_b32_e32 v127, v6
	v_mov_b32_e32 v128, v6
	v_mov_b32_e32 v129, v6
	v_mov_b32_e32 v130, v6
	v_mov_b32_e32 v131, v6
	v_mov_b32_e32 v80, v6
	v_mov_b32_e32 v81, v6
	v_mov_b32_e32 v82, v6
	v_mov_b32_e32 v83, v6
	v_mov_b32_e32 v84, v6
	v_mov_b32_e32 v85, v6
	v_mov_b32_e32 v86, v6
	v_mov_b32_e32 v87, v6
	v_mov_b32_e32 v100, v6
	v_mov_b32_e32 v101, v6
	v_mov_b32_e32 v102, v6
	v_mov_b32_e32 v103, v6
	v_mov_b32_e32 v104, v6
	v_mov_b32_e32 v105, v6
	v_mov_b32_e32 v106, v6
	v_mov_b32_e32 v107, v6
	v_mov_b32_e32 v116, v6
	v_mov_b32_e32 v117, v6
	v_mov_b32_e32 v118, v6
	v_mov_b32_e32 v119, v6
	v_mov_b32_e32 v120, v6
	v_mov_b32_e32 v121, v6
	v_mov_b32_e32 v122, v6
	v_mov_b32_e32 v123, v6
	v_mov_b32_e32 v132, v6
	v_mov_b32_e32 v133, v6
	v_mov_b32_e32 v134, v6
	v_mov_b32_e32 v135, v6
	v_mov_b32_e32 v136, v6
	v_mov_b32_e32 v137, v6
	v_mov_b32_e32 v138, v6
	v_mov_b32_e32 v139, v6
	.p2alignl 6, 3212836864
